# vt8fuse + guhoist: gate/up epilogue bias loads issued in the unit's last K iteration (registers), epilogue head waits removed (one vmcnt(8) before the gather results' use)
# speedup vs baseline: 1.0010x; 1.0010x over previous
.LBB0_697:
	s_cmp_eq_u32 s39, 4
	s_cbranch_scc0 .Lgh_0
	s_lshl_b32 s100, s38, 13
	s_add_u32 s100, s20, s100
	s_addc_u32 s101, s21, 0
	v_lshl_or_b32 v240, s28, 7, v199
	v_mov_b32_e32 v241, 0
	v_lshl_add_u64 v[240:241], v[240:241], 2, s[100:101]
	global_load_dwordx4 v[224:227], v[240:241], off
	global_load_dwordx4 v[228:231], v[240:241], off offset:16
	s_mov_b32 s100, s84
	s_mov_b32 s101, 0
	v_lshl_add_u64 v[242:243], v[240:241], 0, s[100:101]
	global_load_dwordx4 v[232:235], v[242:243], off
	v_lshl_add_u64 v[242:243], v[240:241], 0, s[50:51]
	global_load_dwordx4 v[236:239], v[242:243], off offset:16

.LBB0_716:
	s_ashr_i32 s39, s38, 31
	s_lshl_b64 s[66:67], s[38:39], 13
	v_lshl_or_b32 v20, s28, 7, v199
	s_add_u32 s66, s20, s66
	s_addc_u32 s67, s21, s67
	v_ashrrev_i32_e32 v21, 31, v20
	v_lshl_add_u64 v[6:7], v[20:21], 2, s[66:67]
	s_waitcnt vmcnt(6)
	v_mov_b32_e32 v14, v224
	v_mov_b32_e32 v15, v225
	v_mov_b32_e32 v16, v226
	v_mov_b32_e32 v17, v227
	v_mov_b32_e32 v10, v228
	v_mov_b32_e32 v11, v229
	v_mov_b32_e32 v12, v230
	v_mov_b32_e32 v13, v231
	v_add_co_u32_e32 v2, vcc, s84, v6
	v_mov_b32_e32 v25, 0
	s_nop 0
	v_addc_co_u32_e32 v3, vcc, 0, v7, vcc
	v_lshl_add_u64 v[6:7], v[6:7], 0, s[50:51]
	v_mov_b32_e32 v2, v232
	v_mov_b32_e32 v3, v233
	v_mov_b32_e32 v4, v234
	v_mov_b32_e32 v5, v235
	v_mov_b32_e32 v24, 0
	v_mov_b32_e32 v6, v236
	v_mov_b32_e32 v7, v237
	v_mov_b32_e32 v8, v238
	v_mov_b32_e32 v9, v239
	v_lshl_add_u32 v22, v210, 8, v198
	v_ashrrev_i32_e32 v23, 31, v22
	v_lshlrev_b64 v[18:19], 10, v[22:23]
	v_lshl_add_u64 v[18:19], s[46:47], 0, v[18:19]
	v_lshl_add_u64 v[18:19], v[18:19], 0, v[20:21]
	v_or_b32_e32 v26, 16, v22
	v_ashrrev_i32_e32 v27, 31, v26
	v_pk_fma_f32 v[30:31], v[190:191], s[54:55], v[14:15] op_sel_hi:[1,0,1]
	v_pk_fma_f32 v[34:35], v[186:187], s[54:55], v[10:11] op_sel_hi:[1,0,1]
	v_pk_fma_f32 v[32:33], v[188:189], s[54:55], v[12:13] op_sel_hi:[1,0,1]
	v_min_f32_e32 v34, 0x40e00000, v34
	v_min_f32_e32 v35, 0x40e00000, v35
	v_pk_mul_f32 v[56:57], v[34:35], s[56:57] op_sel_hi:[1,0]
	v_min_f32_e32 v30, 0x40e00000, v30
	v_exp_f32_e32 v56, v56
	v_exp_f32_e32 v57, v57
	v_min_f32_e32 v31, 0x40e00000, v31
	v_min_f32_e32 v32, 0x40e00000, v32
	v_min_f32_e32 v33, 0x40e00000, v33
	v_pk_mul_f32 v[52:53], v[30:31], s[56:57] op_sel_hi:[1,0]
	v_pk_mul_f32 v[58:59], v[32:33], s[56:57] op_sel_hi:[1,0]
	v_exp_f32_e32 v52, v52
	v_exp_f32_e32 v53, v53
	v_exp_f32_e32 v58, v58
	v_exp_f32_e32 v59, v59
	v_pk_add_f32 v[56:57], v[56:57], 1.0 op_sel_hi:[1,0]
	v_pk_fma_f32 v[28:29], v[192:193], s[54:55], v[16:17] op_sel_hi:[1,0,1]
	v_rcp_f32_e32 v56, v56
	v_rcp_f32_e32 v57, v57
	v_min_f32_e32 v28, 0x40e00000, v28
	v_min_f32_e32 v29, 0x40e00000, v29
	v_pk_fma_f32 v[50:51], v[154:155], s[54:55], v[6:7] op_sel_hi:[1,0,1]
	v_pk_mul_f32 v[54:55], v[28:29], s[56:57] op_sel_hi:[1,0]
	v_pk_add_f32 v[52:53], v[52:53], 1.0 op_sel_hi:[1,0]
	v_exp_f32_e32 v54, v54
	v_exp_f32_e32 v55, v55
	v_med3_f32 v50, v50, s85, v203
	v_med3_f32 v51, v51, s85, v203
	v_pk_add_f32 v[58:59], v[58:59], 1.0 op_sel_hi:[1,0]
	v_rcp_f32_e32 v52, v52
	v_rcp_f32_e32 v53, v53
	v_pk_add_f32 v[50:51], v[50:51], 1.0 op_sel_hi:[1,0]
	v_rcp_f32_e32 v58, v58
	v_rcp_f32_e32 v59, v59
	v_pk_mul_f32 v[34:35], v[34:35], v[56:57]
	v_pk_fma_f32 v[46:47], v[158:159], s[54:55], v[2:3] op_sel_hi:[1,0,1]
	v_pk_mul_f32 v[34:35], v[50:51], v[34:35]
	v_pk_fma_f32 v[48:49], v[156:157], s[54:55], v[8:9] op_sel_hi:[1,0,1]
	v_med3_f32 v46, v46, s85, v203
	v_med3_f32 v47, v47, s85, v203
	v_cvt_pk_fp8_f32 v25, v34, v35
	v_pk_fma_f32 v[38:39], v[182:183], s[54:55], v[14:15] op_sel_hi:[1,0,1]
	v_med3_f32 v48, v48, s85, v203
	v_med3_f32 v49, v49, s85, v203
	v_pk_add_f32 v[46:47], v[46:47], 1.0 op_sel_hi:[1,0]
	v_pk_add_f32 v[54:55], v[54:55], 1.0 op_sel_hi:[1,0]
	v_pk_mul_f32 v[30:31], v[30:31], v[52:53]
	v_min_f32_e32 v38, 0x40e00000, v38
	v_min_f32_e32 v39, 0x40e00000, v39
	v_pk_add_f32 v[48:49], v[48:49], 1.0 op_sel_hi:[1,0]
	v_rcp_f32_e32 v54, v54
	v_rcp_f32_e32 v55, v55
	v_pk_mul_f32 v[32:33], v[32:33], v[58:59]
	v_pk_mul_f32 v[30:31], v[46:47], v[30:31]
	v_pk_fma_f32 v[36:37], v[184:185], s[54:55], v[16:17] op_sel_hi:[1,0,1]
	v_pk_mul_f32 v[218:219], v[38:39], s[56:57] op_sel_hi:[1,0]
	v_cvt_pk_fp8_f32 v24, v30, v31
	v_pk_mul_f32 v[30:31], v[48:49], v[32:33]
	v_pk_fma_f32 v[44:45], v[160:161], s[54:55], v[4:5] op_sel_hi:[1,0,1]
	v_exp_f32_e32 v218, v218
	v_exp_f32_e32 v219, v219
	v_cvt_pk_fp8_f32 v25, v30, v31 op_sel:[0,0,1]
	v_min_f32_e32 v30, 0x40e00000, v36
	v_min_f32_e32 v31, 0x40e00000, v37
	v_med3_f32 v44, v44, s85, v203
	v_med3_f32 v45, v45, s85, v203
	v_pk_mul_f32 v[32:33], v[30:31], s[56:57] op_sel_hi:[1,0]
	v_pk_add_f32 v[44:45], v[44:45], 1.0 op_sel_hi:[1,0]
	v_pk_mul_f32 v[28:29], v[28:29], v[54:55]
	v_exp_f32_e32 v32, v32
	v_exp_f32_e32 v33, v33
	v_pk_mul_f32 v[28:29], v[44:45], v[28:29]
	v_pk_fma_f32 v[42:43], v[178:179], s[54:55], v[10:11] op_sel_hi:[1,0,1]
	v_cvt_pk_fp8_f32 v24, v28, v29 op_sel:[0,0,1]
	v_pk_add_f32 v[28:29], v[218:219], 1.0 op_sel_hi:[1,0]
	v_pk_add_f32 v[32:33], v[32:33], 1.0 op_sel_hi:[1,0]
	v_rcp_f32_e32 v28, v28
	v_rcp_f32_e32 v29, v29
	v_min_f32_e32 v34, 0x40e00000, v42
	v_min_f32_e32 v35, 0x40e00000, v43
	v_pk_fma_f32 v[62:63], v[150:151], s[54:55], v[2:3] op_sel_hi:[1,0,1]
	v_rcp_f32_e32 v32, v32
	v_rcp_f32_e32 v33, v33
	v_pk_mul_f32 v[36:37], v[34:35], s[56:57] op_sel_hi:[1,0]
	v_med3_f32 v62, v62, s85, v203
	v_med3_f32 v63, v63, s85, v203
	v_exp_f32_e32 v36, v36
	v_exp_f32_e32 v37, v37
	v_pk_fma_f32 v[60:61], v[152:153], s[54:55], v[4:5] op_sel_hi:[1,0,1]
	global_store_dwordx2 v[18:19], v[24:25], off
	v_pk_add_f32 v[24:25], v[62:63], 1.0 op_sel_hi:[1,0]
	v_pk_mul_f32 v[28:29], v[38:39], v[28:29]
	v_pk_mul_f32 v[30:31], v[30:31], v[32:33]
	v_pk_mul_f32 v[24:25], v[24:25], v[28:29]
	v_med3_f32 v28, v60, s85, v203
	v_med3_f32 v29, v61, s85, v203
	v_pk_add_f32 v[28:29], v[28:29], 1.0 op_sel_hi:[1,0]
	v_pk_fma_f32 v[40:41], v[180:181], s[54:55], v[12:13] op_sel_hi:[1,0,1]
	v_pk_mul_f32 v[28:29], v[28:29], v[30:31]
	v_pk_add_f32 v[30:31], v[36:37], 1.0 op_sel_hi:[1,0]
	v_mov_b32_e32 v38, 0
	v_rcp_f32_e32 v30, v30
	v_rcp_f32_e32 v31, v31
	v_cvt_pk_fp8_f32 v38, v24, v25
	v_pk_fma_f32 v[216:217], v[146:147], s[54:55], v[6:7] op_sel_hi:[1,0,1]
	v_mov_b32_e32 v39, 0
	v_pk_mul_f32 v[30:31], v[34:35], v[30:31]
	v_min_f32_e32 v34, 0x40e00000, v40
	v_min_f32_e32 v35, 0x40e00000, v41
	v_pk_mul_f32 v[36:37], v[34:35], s[56:57] op_sel_hi:[1,0]
	v_cvt_pk_fp8_f32 v38, v28, v29 op_sel:[0,0,1]
	v_exp_f32_e32 v36, v36
	v_exp_f32_e32 v37, v37
	v_pk_fma_f32 v[28:29], v[174:175], s[54:55], v[14:15] op_sel_hi:[1,0,1]
	v_med3_f32 v32, v216, s85, v203
	v_min_f32_e32 v28, 0x40e00000, v28
	v_pk_add_f32 v[36:37], v[36:37], 1.0 op_sel_hi:[1,0]
	v_min_f32_e32 v29, 0x40e00000, v29
	v_rcp_f32_e32 v36, v36
	v_rcp_f32_e32 v37, v37
	v_med3_f32 v33, v217, s85, v203
	v_pk_add_f32 v[32:33], v[32:33], 1.0 op_sel_hi:[1,0]
	v_pk_fma_f32 v[64:65], v[148:149], s[54:55], v[8:9] op_sel_hi:[1,0,1]
	v_pk_mul_f32 v[24:25], v[34:35], v[36:37]
	v_pk_mul_f32 v[36:37], v[28:29], s[56:57] op_sel_hi:[1,0]
	v_pk_mul_f32 v[30:31], v[32:33], v[30:31]
	v_exp_f32_e32 v36, v36
	v_exp_f32_e32 v37, v37
	v_cvt_pk_fp8_f32 v39, v30, v31
	v_med3_f32 v32, v64, s85, v203
	v_med3_f32 v33, v65, s85, v203
	v_pk_add_f32 v[36:37], v[36:37], 1.0 op_sel_hi:[1,0]
	v_pk_add_f32 v[32:33], v[32:33], 1.0 op_sel_hi:[1,0]
	v_rcp_f32_e32 v36, v36
	v_rcp_f32_e32 v37, v37
	v_pk_mul_f32 v[24:25], v[32:33], v[24:25]
	v_pk_fma_f32 v[32:33], v[170:171], s[54:55], v[10:11] op_sel_hi:[1,0,1]
	v_cvt_pk_fp8_f32 v39, v24, v25 op_sel:[0,0,1]
	v_lshlrev_b64 v[24:25], 10, v[26:27]
	v_pk_fma_f32 v[26:27], v[176:177], s[54:55], v[16:17] op_sel_hi:[1,0,1]
	v_pk_mul_f32 v[28:29], v[28:29], v[36:37]
	v_min_f32_e32 v26, 0x40e00000, v26
	v_min_f32_e32 v27, 0x40e00000, v27
	v_pk_mul_f32 v[36:37], v[26:27], s[56:57] op_sel_hi:[1,0]
	v_lshl_add_u64 v[24:25], s[46:47], 0, v[24:25]
	v_exp_f32_e32 v36, v36
	v_exp_f32_e32 v37, v37
	v_lshl_add_u64 v[24:25], v[24:25], 0, v[20:21]
	global_store_dwordx2 v[24:25], v[38:39], off
	v_pk_fma_f32 v[38:39], v[142:143], s[54:55], v[2:3] op_sel_hi:[1,0,1]
	v_pk_add_f32 v[36:37], v[36:37], 1.0 op_sel_hi:[1,0]
	v_med3_f32 v38, v38, s85, v203
	v_med3_f32 v39, v39, s85, v203
	v_pk_add_f32 v[38:39], v[38:39], 1.0 op_sel_hi:[1,0]
	v_min_f32_e32 v32, 0x40e00000, v32
	v_min_f32_e32 v33, 0x40e00000, v33
	v_pk_mul_f32 v[28:29], v[38:39], v[28:29]
	v_rcp_f32_e32 v36, v36
	v_rcp_f32_e32 v37, v37
	v_pk_mul_f32 v[38:39], v[32:33], s[56:57] op_sel_hi:[1,0]
	v_pk_fma_f32 v[34:35], v[144:145], s[54:55], v[4:5] op_sel_hi:[1,0,1]
	v_exp_f32_e32 v38, v38
	v_exp_f32_e32 v39, v39
	v_med3_f32 v34, v34, s85, v203
	v_med3_f32 v35, v35, s85, v203
	v_pk_add_f32 v[34:35], v[34:35], 1.0 op_sel_hi:[1,0]
	v_pk_mul_f32 v[26:27], v[26:27], v[36:37]
	v_pk_fma_f32 v[30:31], v[172:173], s[54:55], v[12:13] op_sel_hi:[1,0,1]
	v_pk_mul_f32 v[26:27], v[34:35], v[26:27]
	v_pk_add_f32 v[34:35], v[38:39], 1.0 op_sel_hi:[1,0]
	v_min_f32_e32 v30, 0x40e00000, v30
	v_rcp_f32_e32 v34, v34
	v_rcp_f32_e32 v35, v35
	v_min_f32_e32 v31, 0x40e00000, v31
	v_mov_b32_e32 v38, 0
	v_cvt_pk_fp8_f32 v38, v28, v29
	v_pk_mul_f32 v[32:33], v[32:33], v[34:35]
	v_pk_mul_f32 v[34:35], v[30:31], s[56:57] op_sel_hi:[1,0]
	v_pk_fma_f32 v[42:43], v[138:139], s[54:55], v[6:7] op_sel_hi:[1,0,1]
	v_exp_f32_e32 v34, v34
	v_exp_f32_e32 v35, v35
	v_med3_f32 v36, v42, s85, v203
	v_med3_f32 v37, v43, s85, v203
	v_pk_add_f32 v[36:37], v[36:37], 1.0 op_sel_hi:[1,0]
	v_pk_add_f32 v[34:35], v[34:35], 1.0 op_sel_hi:[1,0]
	v_cvt_pk_fp8_f32 v38, v26, v27 op_sel:[0,0,1]
	v_rcp_f32_e32 v34, v34
	v_rcp_f32_e32 v35, v35
	v_pk_fma_f32 v[26:27], v[166:167], s[54:55], v[14:15] op_sel_hi:[1,0,1]
	v_pk_mul_f32 v[32:33], v[36:37], v[32:33]
	v_mov_b32_e32 v39, 0
	v_min_f32_e32 v26, 0x40e00000, v26
	v_min_f32_e32 v27, 0x40e00000, v27
	v_pk_fma_f32 v[40:41], v[140:141], s[54:55], v[8:9] op_sel_hi:[1,0,1]
	v_cvt_pk_fp8_f32 v39, v32, v33
	v_pk_mul_f32 v[28:29], v[30:31], v[34:35]
	v_pk_mul_f32 v[34:35], v[26:27], s[56:57] op_sel_hi:[1,0]
	v_med3_f32 v36, v40, s85, v203
	v_med3_f32 v37, v41, s85, v203
	v_exp_f32_e32 v34, v34
	v_exp_f32_e32 v35, v35
	v_pk_add_f32 v[36:37], v[36:37], 1.0 op_sel_hi:[1,0]
	v_or_b32_e32 v24, 32, v22
	v_pk_mul_f32 v[28:29], v[36:37], v[28:29]
	v_ashrrev_i32_e32 v25, 31, v24
	v_cvt_pk_fp8_f32 v39, v28, v29 op_sel:[0,0,1]
	v_lshlrev_b64 v[24:25], 10, v[24:25]
	v_pk_add_f32 v[34:35], v[34:35], 1.0 op_sel_hi:[1,0]
	v_lshl_add_u64 v[24:25], s[46:47], 0, v[24:25]
	v_rcp_f32_e32 v34, v34
	v_rcp_f32_e32 v35, v35
	v_lshl_add_u64 v[24:25], v[24:25], 0, v[20:21]
	global_store_dwordx2 v[24:25], v[38:39], off
	v_pk_fma_f32 v[24:25], v[168:169], s[54:55], v[16:17] op_sel_hi:[1,0,1]
	v_pk_mul_f32 v[26:27], v[26:27], v[34:35]
	v_min_f32_e32 v24, 0x40e00000, v24
	v_min_f32_e32 v25, 0x40e00000, v25
	v_pk_mul_f32 v[34:35], v[24:25], s[56:57] op_sel_hi:[1,0]
	v_pk_fma_f32 v[36:37], v[134:135], s[54:55], v[2:3] op_sel_hi:[1,0,1]
	v_exp_f32_e32 v34, v34
	v_exp_f32_e32 v35, v35
	v_pk_fma_f32 v[30:31], v[162:163], s[54:55], v[10:11] op_sel_hi:[1,0,1]
	v_med3_f32 v36, v36, s85, v203
	v_med3_f32 v37, v37, s85, v203
	v_pk_add_f32 v[36:37], v[36:37], 1.0 op_sel_hi:[1,0]
	v_pk_add_f32 v[34:35], v[34:35], 1.0 op_sel_hi:[1,0]
	v_min_f32_e32 v30, 0x40e00000, v30
	v_min_f32_e32 v31, 0x40e00000, v31
	v_pk_mul_f32 v[26:27], v[36:37], v[26:27]
	v_rcp_f32_e32 v34, v34
	v_rcp_f32_e32 v35, v35
	v_pk_mul_f32 v[36:37], v[30:31], s[56:57] op_sel_hi:[1,0]
	v_pk_fma_f32 v[32:33], v[136:137], s[54:55], v[4:5] op_sel_hi:[1,0,1]
	v_exp_f32_e32 v36, v36
	v_exp_f32_e32 v37, v37
	v_med3_f32 v32, v32, s85, v203
	v_med3_f32 v33, v33, s85, v203
	v_pk_add_f32 v[32:33], v[32:33], 1.0 op_sel_hi:[1,0]
	v_pk_mul_f32 v[24:25], v[24:25], v[34:35]
	v_pk_fma_f32 v[28:29], v[164:165], s[54:55], v[12:13] op_sel_hi:[1,0,1]
	v_pk_mul_f32 v[24:25], v[32:33], v[24:25]
	v_pk_add_f32 v[32:33], v[36:37], 1.0 op_sel_hi:[1,0]
	v_min_f32_e32 v28, 0x40e00000, v28
	v_rcp_f32_e32 v32, v32
	v_rcp_f32_e32 v33, v33
	v_min_f32_e32 v29, 0x40e00000, v29
	v_or_b32_e32 v22, 48, v22
	v_ashrrev_i32_e32 v23, 31, v22
	v_pk_mul_f32 v[30:31], v[30:31], v[32:33]
	v_pk_mul_f32 v[32:33], v[28:29], s[56:57] op_sel_hi:[1,0]
	v_pk_fma_f32 v[40:41], v[130:131], s[54:55], v[6:7] op_sel_hi:[1,0,1]
	v_exp_f32_e32 v32, v32
	v_exp_f32_e32 v33, v33
	v_lshlrev_b64 v[22:23], 10, v[22:23]
	v_med3_f32 v34, v40, s85, v203
	v_med3_f32 v35, v41, s85, v203
	v_pk_add_f32 v[32:33], v[32:33], 1.0 op_sel_hi:[1,0]
	v_lshl_add_u64 v[22:23], s[46:47], 0, v[22:23]
	v_pk_add_f32 v[34:35], v[34:35], 1.0 op_sel_hi:[1,0]
	v_rcp_f32_e32 v32, v32
	v_rcp_f32_e32 v33, v33
	v_lshl_add_u64 v[20:21], v[22:23], 0, v[20:21]
	v_pk_fma_f32 v[22:23], v[126:127], s[54:55], v[14:15] op_sel_hi:[1,0,1]
	v_pk_mul_f32 v[30:31], v[34:35], v[30:31]
	v_mov_b32_e32 v36, 0
	v_mov_b32_e32 v37, 0
	v_min_f32_e32 v22, 0x40e00000, v22
	v_min_f32_e32 v23, 0x40e00000, v23
	v_pk_fma_f32 v[38:39], v[132:133], s[54:55], v[8:9] op_sel_hi:[1,0,1]
	v_cvt_pk_fp8_f32 v36, v26, v27
	v_cvt_pk_fp8_f32 v37, v30, v31
	v_pk_mul_f32 v[30:31], v[22:23], s[56:57] op_sel_hi:[1,0]
	v_med3_f32 v34, v38, s85, v203
	v_med3_f32 v35, v39, s85, v203
	v_exp_f32_e32 v30, v30
	v_exp_f32_e32 v31, v31
	v_pk_add_f32 v[34:35], v[34:35], 1.0 op_sel_hi:[1,0]
	v_pk_mul_f32 v[26:27], v[28:29], v[32:33]
	v_cvt_pk_fp8_f32 v36, v24, v25 op_sel:[0,0,1]
	v_pk_mul_f32 v[26:27], v[34:35], v[26:27]
	v_pk_add_f32 v[30:31], v[30:31], 1.0 op_sel_hi:[1,0]
	v_cvt_pk_fp8_f32 v37, v26, v27 op_sel:[0,0,1]
	v_rcp_f32_e32 v30, v30
	v_rcp_f32_e32 v31, v31
	v_pk_fma_f32 v[32:33], v[94:95], s[54:55], v[2:3] op_sel_hi:[1,0,1]
	global_store_dwordx2 v[20:21], v[36:37], off
	v_pk_fma_f32 v[20:21], v[128:129], s[54:55], v[16:17] op_sel_hi:[1,0,1]
	v_pk_mul_f32 v[22:23], v[22:23], v[30:31]
	v_min_f32_e32 v20, 0x40e00000, v20
	v_min_f32_e32 v21, 0x40e00000, v21
	v_pk_mul_f32 v[30:31], v[20:21], s[56:57] op_sel_hi:[1,0]
	v_pk_fma_f32 v[26:27], v[122:123], s[54:55], v[10:11] op_sel_hi:[1,0,1]
	v_exp_f32_e32 v30, v30
	v_exp_f32_e32 v31, v31
	v_med3_f32 v32, v32, s85, v203
	v_med3_f32 v33, v33, s85, v203
	v_pk_add_f32 v[32:33], v[32:33], 1.0 op_sel_hi:[1,0]
	v_pk_add_f32 v[30:31], v[30:31], 1.0 op_sel_hi:[1,0]
	v_min_f32_e32 v26, 0x40e00000, v26
	v_min_f32_e32 v27, 0x40e00000, v27
	v_pk_mul_f32 v[22:23], v[32:33], v[22:23]
	v_rcp_f32_e32 v30, v30
	v_rcp_f32_e32 v31, v31
	v_pk_mul_f32 v[32:33], v[26:27], s[56:57] op_sel_hi:[1,0]
	v_pk_fma_f32 v[28:29], v[96:97], s[54:55], v[4:5] op_sel_hi:[1,0,1]
	v_exp_f32_e32 v32, v32
	v_exp_f32_e32 v33, v33
	v_med3_f32 v28, v28, s85, v203
	v_med3_f32 v29, v29, s85, v203
	v_pk_add_f32 v[28:29], v[28:29], 1.0 op_sel_hi:[1,0]
	v_pk_mul_f32 v[20:21], v[20:21], v[30:31]
	v_pk_fma_f32 v[24:25], v[124:125], s[54:55], v[12:13] op_sel_hi:[1,0,1]
	v_pk_mul_f32 v[20:21], v[28:29], v[20:21]
	v_pk_add_f32 v[28:29], v[32:33], 1.0 op_sel_hi:[1,0]
	v_min_f32_e32 v24, 0x40e00000, v24
	v_rcp_f32_e32 v28, v28
	v_rcp_f32_e32 v29, v29
	v_min_f32_e32 v25, 0x40e00000, v25
	v_pk_fma_f32 v[36:37], v[90:91], s[54:55], v[6:7] op_sel_hi:[1,0,1]
	v_mov_b32_e32 v33, 0
	v_pk_mul_f32 v[26:27], v[26:27], v[28:29]
	v_pk_mul_f32 v[28:29], v[24:25], s[56:57] op_sel_hi:[1,0]
	v_med3_f32 v30, v36, s85, v203
	v_exp_f32_e32 v28, v28
	v_exp_f32_e32 v29, v29
	v_med3_f32 v31, v37, s85, v203
	v_pk_add_f32 v[30:31], v[30:31], 1.0 op_sel_hi:[1,0]
	v_pk_fma_f32 v[34:35], v[92:93], s[54:55], v[8:9] op_sel_hi:[1,0,1]
	v_pk_add_f32 v[28:29], v[28:29], 1.0 op_sel_hi:[1,0]
	v_pk_mul_f32 v[26:27], v[30:31], v[26:27]
	v_rcp_f32_e32 v28, v28
	v_rcp_f32_e32 v29, v29
	v_cvt_pk_fp8_f32 v33, v26, v27
	v_med3_f32 v30, v34, s85, v203
	v_med3_f32 v31, v35, s85, v203
	v_mov_b32_e32 v32, 0
	v_pk_add_f32 v[30:31], v[30:31], 1.0 op_sel_hi:[1,0]
	v_cvt_pk_fp8_f32 v32, v22, v23
	v_pk_mul_f32 v[22:23], v[24:25], v[28:29]
	v_pk_fma_f32 v[26:27], v[114:115], s[54:55], v[10:11] op_sel_hi:[1,0,1]
	v_pk_mul_f32 v[22:23], v[30:31], v[22:23]
	v_cvt_pk_fp8_f32 v32, v20, v21 op_sel:[0,0,1]
	v_cvt_pk_fp8_f32 v33, v22, v23 op_sel:[0,0,1]
	v_pk_fma_f32 v[22:23], v[118:119], s[54:55], v[14:15] op_sel_hi:[1,0,1]
	v_add_co_u32_e32 v20, vcc, s83, v18
	v_min_f32_e32 v22, 0x40e00000, v22
	v_min_f32_e32 v23, 0x40e00000, v23
	v_pk_mul_f32 v[30:31], v[22:23], s[56:57] op_sel_hi:[1,0]
	v_addc_co_u32_e32 v21, vcc, 0, v19, vcc
	v_exp_f32_e32 v30, v30
	v_exp_f32_e32 v31, v31
	global_store_dwordx2 v[20:21], v[32:33], off
	v_pk_fma_f32 v[20:21], v[120:121], s[54:55], v[16:17] op_sel_hi:[1,0,1]
	v_pk_fma_f32 v[32:33], v[86:87], s[54:55], v[2:3] op_sel_hi:[1,0,1]
	v_pk_add_f32 v[30:31], v[30:31], 1.0 op_sel_hi:[1,0]
	v_min_f32_e32 v20, 0x40e00000, v20
	v_rcp_f32_e32 v30, v30
	v_rcp_f32_e32 v31, v31
	v_min_f32_e32 v21, 0x40e00000, v21
	v_med3_f32 v32, v32, s85, v203
	v_med3_f32 v33, v33, s85, v203
	v_pk_mul_f32 v[22:23], v[22:23], v[30:31]
	v_pk_mul_f32 v[30:31], v[20:21], s[56:57] op_sel_hi:[1,0]
	v_pk_add_f32 v[32:33], v[32:33], 1.0 op_sel_hi:[1,0]
	v_exp_f32_e32 v30, v30
	v_exp_f32_e32 v31, v31
	v_min_f32_e32 v26, 0x40e00000, v26
	v_min_f32_e32 v27, 0x40e00000, v27
	v_pk_mul_f32 v[22:23], v[32:33], v[22:23]
	v_pk_add_f32 v[30:31], v[30:31], 1.0 op_sel_hi:[1,0]
	v_pk_mul_f32 v[32:33], v[26:27], s[56:57] op_sel_hi:[1,0]
	v_rcp_f32_e32 v30, v30
	v_rcp_f32_e32 v31, v31
	v_exp_f32_e32 v32, v32
	v_exp_f32_e32 v33, v33
	v_pk_fma_f32 v[28:29], v[88:89], s[54:55], v[4:5] op_sel_hi:[1,0,1]
	v_pk_mul_f32 v[20:21], v[20:21], v[30:31]
	v_med3_f32 v28, v28, s85, v203
	v_med3_f32 v29, v29, s85, v203
	v_pk_add_f32 v[28:29], v[28:29], 1.0 op_sel_hi:[1,0]
	v_pk_fma_f32 v[24:25], v[116:117], s[54:55], v[12:13] op_sel_hi:[1,0,1]
	v_pk_mul_f32 v[20:21], v[28:29], v[20:21]
	v_pk_add_f32 v[28:29], v[32:33], 1.0 op_sel_hi:[1,0]
	v_min_f32_e32 v24, 0x40e00000, v24
	v_rcp_f32_e32 v28, v28
	v_rcp_f32_e32 v29, v29
	v_min_f32_e32 v25, 0x40e00000, v25
	v_pk_fma_f32 v[36:37], v[82:83], s[54:55], v[6:7] op_sel_hi:[1,0,1]
	v_mov_b32_e32 v33, 0
	v_pk_mul_f32 v[26:27], v[26:27], v[28:29]
	v_pk_mul_f32 v[28:29], v[24:25], s[56:57] op_sel_hi:[1,0]
	v_med3_f32 v30, v36, s85, v203
	v_exp_f32_e32 v28, v28
	v_exp_f32_e32 v29, v29
	v_med3_f32 v31, v37, s85, v203
	v_pk_add_f32 v[30:31], v[30:31], 1.0 op_sel_hi:[1,0]
	v_pk_fma_f32 v[34:35], v[84:85], s[54:55], v[8:9] op_sel_hi:[1,0,1]
	v_pk_add_f32 v[28:29], v[28:29], 1.0 op_sel_hi:[1,0]
	v_pk_mul_f32 v[26:27], v[30:31], v[26:27]
	v_rcp_f32_e32 v28, v28
	v_rcp_f32_e32 v29, v29
	v_cvt_pk_fp8_f32 v33, v26, v27
	v_med3_f32 v30, v34, s85, v203
	v_med3_f32 v31, v35, s85, v203
	v_mov_b32_e32 v32, 0
	v_pk_add_f32 v[30:31], v[30:31], 1.0 op_sel_hi:[1,0]
	v_cvt_pk_fp8_f32 v32, v22, v23
	v_pk_mul_f32 v[22:23], v[24:25], v[28:29]
	v_pk_fma_f32 v[26:27], v[106:107], s[54:55], v[10:11] op_sel_hi:[1,0,1]
	v_pk_mul_f32 v[22:23], v[30:31], v[22:23]
	v_cvt_pk_fp8_f32 v32, v20, v21 op_sel:[0,0,1]
	v_cvt_pk_fp8_f32 v33, v22, v23 op_sel:[0,0,1]
	v_pk_fma_f32 v[22:23], v[110:111], s[54:55], v[14:15] op_sel_hi:[1,0,1]
	v_add_co_u32_e32 v20, vcc, s86, v18
	v_min_f32_e32 v22, 0x40e00000, v22
	v_min_f32_e32 v23, 0x40e00000, v23
	v_pk_mul_f32 v[30:31], v[22:23], s[56:57] op_sel_hi:[1,0]
	v_addc_co_u32_e32 v21, vcc, 0, v19, vcc
	v_exp_f32_e32 v30, v30
	v_exp_f32_e32 v31, v31
	global_store_dwordx2 v[20:21], v[32:33], off
	v_pk_fma_f32 v[20:21], v[112:113], s[54:55], v[16:17] op_sel_hi:[1,0,1]
	v_pk_fma_f32 v[32:33], v[78:79], s[54:55], v[2:3] op_sel_hi:[1,0,1]
	v_pk_add_f32 v[30:31], v[30:31], 1.0 op_sel_hi:[1,0]
	v_min_f32_e32 v20, 0x40e00000, v20
	v_rcp_f32_e32 v30, v30
	v_rcp_f32_e32 v31, v31
	v_min_f32_e32 v21, 0x40e00000, v21
	v_med3_f32 v32, v32, s85, v203
	v_med3_f32 v33, v33, s85, v203
	v_pk_mul_f32 v[22:23], v[22:23], v[30:31]
	v_pk_mul_f32 v[30:31], v[20:21], s[56:57] op_sel_hi:[1,0]
	v_pk_add_f32 v[32:33], v[32:33], 1.0 op_sel_hi:[1,0]
	v_exp_f32_e32 v30, v30
	v_exp_f32_e32 v31, v31
	v_min_f32_e32 v26, 0x40e00000, v26
	v_min_f32_e32 v27, 0x40e00000, v27
	v_pk_mul_f32 v[22:23], v[32:33], v[22:23]
	v_pk_add_f32 v[30:31], v[30:31], 1.0 op_sel_hi:[1,0]
	v_pk_mul_f32 v[32:33], v[26:27], s[56:57] op_sel_hi:[1,0]
	v_rcp_f32_e32 v30, v30
	v_rcp_f32_e32 v31, v31
	v_exp_f32_e32 v32, v32
	v_exp_f32_e32 v33, v33
	v_pk_fma_f32 v[28:29], v[80:81], s[54:55], v[4:5] op_sel_hi:[1,0,1]
	v_pk_mul_f32 v[20:21], v[20:21], v[30:31]
	v_med3_f32 v28, v28, s85, v203
	v_med3_f32 v29, v29, s85, v203
	v_pk_add_f32 v[28:29], v[28:29], 1.0 op_sel_hi:[1,0]
	v_pk_fma_f32 v[24:25], v[108:109], s[54:55], v[12:13] op_sel_hi:[1,0,1]
	v_pk_mul_f32 v[20:21], v[28:29], v[20:21]
	v_pk_add_f32 v[28:29], v[32:33], 1.0 op_sel_hi:[1,0]
	v_min_f32_e32 v24, 0x40e00000, v24
	v_rcp_f32_e32 v28, v28
	v_rcp_f32_e32 v29, v29
	v_min_f32_e32 v25, 0x40e00000, v25
	v_pk_fma_f32 v[36:37], v[74:75], s[54:55], v[6:7] op_sel_hi:[1,0,1]
	v_mov_b32_e32 v32, 0
	v_pk_mul_f32 v[26:27], v[26:27], v[28:29]
	v_pk_mul_f32 v[28:29], v[24:25], s[56:57] op_sel_hi:[1,0]
	v_med3_f32 v30, v36, s85, v203
	v_exp_f32_e32 v28, v28
	v_exp_f32_e32 v29, v29
	v_med3_f32 v31, v37, s85, v203
	v_pk_add_f32 v[30:31], v[30:31], 1.0 op_sel_hi:[1,0]
	v_mov_b32_e32 v33, 0
	v_pk_add_f32 v[28:29], v[28:29], 1.0 op_sel_hi:[1,0]
	v_pk_mul_f32 v[26:27], v[30:31], v[26:27]
	v_rcp_f32_e32 v28, v28
	v_rcp_f32_e32 v29, v29
	v_pk_fma_f32 v[34:35], v[76:77], s[54:55], v[8:9] op_sel_hi:[1,0,1]
	v_cvt_pk_fp8_f32 v32, v22, v23
	v_cvt_pk_fp8_f32 v33, v26, v27
	v_med3_f32 v30, v34, s85, v203
	v_med3_f32 v31, v35, s85, v203
	v_pk_add_f32 v[30:31], v[30:31], 1.0 op_sel_hi:[1,0]
	v_pk_mul_f32 v[22:23], v[24:25], v[28:29]
	v_cvt_pk_fp8_f32 v32, v20, v21 op_sel:[0,0,1]
	v_pk_mul_f32 v[22:23], v[30:31], v[22:23]
	v_add_co_u32_e32 v20, vcc, s87, v18
	v_cvt_pk_fp8_f32 v33, v22, v23 op_sel:[0,0,1]
	v_pk_fma_f32 v[14:15], v[102:103], s[54:55], v[14:15] op_sel_hi:[1,0,1]
	v_addc_co_u32_e32 v21, vcc, 0, v19, vcc
	v_min_f32_e32 v14, 0x40e00000, v14
	v_min_f32_e32 v15, 0x40e00000, v15
	global_store_dwordx2 v[20:21], v[32:33], off
	v_pk_mul_f32 v[20:21], v[14:15], s[56:57] op_sel_hi:[1,0]
	v_pk_fma_f32 v[16:17], v[104:105], s[54:55], v[16:17] op_sel_hi:[1,0,1]
	v_exp_f32_e32 v20, v20
	v_exp_f32_e32 v21, v21
	v_min_f32_e32 v16, 0x40e00000, v16
	v_min_f32_e32 v17, 0x40e00000, v17
	v_pk_fma_f32 v[2:3], v[70:71], s[54:55], v[2:3] op_sel_hi:[1,0,1]
	v_pk_add_f32 v[20:21], v[20:21], 1.0 op_sel_hi:[1,0]
	v_med3_f32 v2, v2, s85, v203
	v_rcp_f32_e32 v20, v20
	v_rcp_f32_e32 v21, v21
	v_med3_f32 v3, v3, s85, v203
	v_pk_fma_f32 v[10:11], v[98:99], s[54:55], v[10:11] op_sel_hi:[1,0,1]
	v_pk_add_f32 v[2:3], v[2:3], 1.0 op_sel_hi:[1,0]
	v_pk_mul_f32 v[14:15], v[14:15], v[20:21]
	v_pk_mul_f32 v[20:21], v[16:17], s[56:57] op_sel_hi:[1,0]
	v_pk_mul_f32 v[2:3], v[2:3], v[14:15]
	v_exp_f32_e32 v20, v20
	v_exp_f32_e32 v21, v21
	v_min_f32_e32 v10, 0x40e00000, v10
	v_min_f32_e32 v11, 0x40e00000, v11
	v_pk_fma_f32 v[4:5], v[72:73], s[54:55], v[4:5] op_sel_hi:[1,0,1]
	v_pk_add_f32 v[14:15], v[20:21], 1.0 op_sel_hi:[1,0]
	v_pk_mul_f32 v[20:21], v[10:11], s[56:57] op_sel_hi:[1,0]
	v_rcp_f32_e32 v14, v14
	v_rcp_f32_e32 v15, v15
	v_exp_f32_e32 v20, v20
	v_exp_f32_e32 v21, v21
	v_med3_f32 v4, v4, s85, v203
	v_med3_f32 v5, v5, s85, v203
	v_pk_add_f32 v[4:5], v[4:5], 1.0 op_sel_hi:[1,0]
	v_pk_mul_f32 v[14:15], v[16:17], v[14:15]
	v_pk_fma_f32 v[12:13], v[100:101], s[54:55], v[12:13] op_sel_hi:[1,0,1]
	v_pk_mul_f32 v[4:5], v[4:5], v[14:15]
	v_pk_add_f32 v[14:15], v[20:21], 1.0 op_sel_hi:[1,0]
	v_min_f32_e32 v12, 0x40e00000, v12
	v_rcp_f32_e32 v14, v14
	v_rcp_f32_e32 v15, v15
	v_min_f32_e32 v13, 0x40e00000, v13
	v_pk_fma_f32 v[6:7], v[66:67], s[54:55], v[6:7] op_sel_hi:[1,0,1]
	v_pk_fma_f32 v[8:9], v[68:69], s[54:55], v[8:9] op_sel_hi:[1,0,1]
	v_pk_mul_f32 v[10:11], v[10:11], v[14:15]
	v_pk_mul_f32 v[14:15], v[12:13], s[56:57] op_sel_hi:[1,0]
	v_med3_f32 v6, v6, s85, v203
	v_exp_f32_e32 v14, v14
	v_exp_f32_e32 v15, v15
	v_med3_f32 v7, v7, s85, v203
	v_pk_add_f32 v[6:7], v[6:7], 1.0 op_sel_hi:[1,0]
	v_med3_f32 v8, v8, s85, v203
	v_pk_mul_f32 v[6:7], v[6:7], v[10:11]
	v_pk_add_f32 v[10:11], v[14:15], 1.0 op_sel_hi:[1,0]
	v_mov_b32_e32 v14, 0
	v_rcp_f32_e32 v10, v10
	v_rcp_f32_e32 v11, v11
	v_mov_b32_e32 v15, 0
	v_cvt_pk_fp8_f32 v14, v2, v3
	v_cvt_pk_fp8_f32 v15, v6, v7
	v_med3_f32 v9, v9, s85, v203
	v_pk_add_f32 v[8:9], v[8:9], 1.0 op_sel_hi:[1,0]
	v_pk_mul_f32 v[2:3], v[12:13], v[10:11]
	v_cvt_pk_fp8_f32 v14, v4, v5 op_sel:[0,0,1]
	v_pk_mul_f32 v[2:3], v[8:9], v[2:3]
	v_mov_b32_e32 v5, v214
	v_cvt_pk_fp8_f32 v15, v2, v3 op_sel:[0,0,1]
	v_add_co_u32_e32 v2, vcc, 0x2c000, v18
	v_mov_b32_e32 v4, v212
	s_nop 0
	v_addc_co_u32_e32 v3, vcc, 0, v19, vcc
	global_store_dwordx2 v[2:3], v[14:15], off
	s_and_b64 vcc, exec, s[4:5]
	v_mov_b32_e32 v2, v213
	v_mov_b32_e32 v3, v211
	s_cbranch_vccnz .LBB0_718
	s_waitcnt vmcnt(8)
	v_mov_b32_e32 v2, v194
	s_nop 0
	v_ashrrev_i32_e32 v3, 31, v2
	v_lshrrev_b32_e32 v3, 26, v3
	v_lshlrev_b32_e32 v4, 4, v2
	v_add_u32_e32 v3, v2, v3
	v_bfe_i32 v2, v2, 27, 1
	v_lshrrev_b32_e32 v2, 22, v2
	v_add_u32_e32 v2, v4, v2
	v_and_b32_e32 v2, 0xfffffc00, v2
	v_sub_u32_e32 v2, v4, v2
	v_lshrrev_b32_e32 v5, 4, v2
	v_bitop3_b32 v5, v5, v2, 32 bitop3:0x6c
	v_ashrrev_i32_e32 v2, 31, v2
	v_lshrrev_b32_e32 v2, 26, v2
	v_add_u32_e32 v2, v5, v2
	v_and_b32_e32 v2, 0xc0, v2
	v_add_u32_e32 v4, 0x2000, v4
	v_sub_u32_e32 v2, v5, v2
	v_ashrrev_i32_e32 v5, 31, v4
	v_lshrrev_b32_e32 v5, 22, v5
	v_add_u32_e32 v5, v4, v5
	v_ashrrev_i32_e32 v5, 10, v5
	v_mul_i32_i24_e32 v6, 0x400, v5
	v_sub_u32_e32 v4, v4, v6
	v_lshrrev_b32_e32 v6, 4, v4
	v_bitop3_b32 v6, v6, v4, 32 bitop3:0x6c
	v_ashrrev_i32_e32 v4, 31, v4
	v_lshrrev_b32_e32 v4, 26, v4
	v_add_u32_e32 v4, v6, v4
	v_and_b32_e32 v4, 0xc0, v4
	v_sub_u32_e32 v4, v6, v4
	v_lshrrev_b32_e32 v3, 1, v3
	v_ashrrev_i16_sdwa v2, v195, sext(v2) dst_sel:DWORD dst_unused:UNUSED_PAD src0_sel:DWORD src1_sel:BYTE_0
	v_lshlrev_b32_e32 v5, 5, v5
	v_ashrrev_i16_sdwa v4, v195, sext(v4) dst_sel:DWORD dst_unused:UNUSED_PAD src0_sel:DWORD src1_sel:BYTE_0
	v_and_b32_e32 v3, 32, v3
	v_bfe_i32 v2, v2, 0, 16
	v_and_b32_e32 v5, 32, v5
	v_bfe_i32 v4, v4, 0, 16
	v_add_lshl_u32 v2, v3, v2, 1
	v_add_lshl_u32 v5, v5, v4, 1
	v_lshl_add_u32 v3, v205, 10, v2
	v_lshl_add_u32 v2, v204, 10, v2
	v_lshl_add_u32 v4, v209, 10, v5
	v_lshl_add_u32 v5, v207, 10, v5

.LBB0_1773:
	s_cmp_eq_u32 s29, 4
	s_cbranch_scc0 .Lgh_1
	s_lshl_b32 s100, s28, 13
	s_add_u32 s100, s72, s100
	s_addc_u32 s101, s73, 0
	v_lshl_or_b32 v240, s20, 7, v198
	v_mov_b32_e32 v241, 0
	v_lshl_add_u64 v[240:241], v[240:241], 2, s[100:101]
	global_load_dwordx4 v[224:227], v[240:241], off
	global_load_dwordx4 v[228:231], v[240:241], off offset:16
	s_mov_b32 s100, s82
	s_mov_b32 s101, 0
	v_lshl_add_u64 v[242:243], v[240:241], 0, s[100:101]
	global_load_dwordx4 v[232:235], v[242:243], off
	v_lshl_add_u64 v[242:243], v[240:241], 0, s[46:47]
	global_load_dwordx4 v[236:239], v[242:243], off offset:16

.LBB0_1792:
	s_ashr_i32 s29, s28, 31
	s_lshl_b64 s[62:63], s[28:29], 13
	v_lshl_or_b32 v20, s20, 7, v198
	s_add_u32 s62, s72, s62
	s_addc_u32 s63, s73, s63
	v_ashrrev_i32_e32 v21, 31, v20
	v_lshl_add_u64 v[6:7], v[20:21], 2, s[62:63]
	s_waitcnt vmcnt(6)
	v_mov_b32_e32 v14, v224
	v_mov_b32_e32 v15, v225
	v_mov_b32_e32 v16, v226
	v_mov_b32_e32 v17, v227
	v_mov_b32_e32 v10, v228
	v_mov_b32_e32 v11, v229
	v_mov_b32_e32 v12, v230
	v_mov_b32_e32 v13, v231
	v_add_co_u32_e32 v2, vcc, s82, v6
	v_mov_b32_e32 v25, 0
	s_nop 0
	v_addc_co_u32_e32 v3, vcc, 0, v7, vcc
	v_lshl_add_u64 v[6:7], v[6:7], 0, s[46:47]
	v_mov_b32_e32 v2, v232
	v_mov_b32_e32 v3, v233
	v_mov_b32_e32 v4, v234
	v_mov_b32_e32 v5, v235
	v_mov_b32_e32 v24, 0
	v_mov_b32_e32 v6, v236
	v_mov_b32_e32 v7, v237
	v_mov_b32_e32 v8, v238
	v_mov_b32_e32 v9, v239
	v_lshl_add_u32 v22, v209, 8, v197
	v_ashrrev_i32_e32 v23, 31, v22
	v_lshlrev_b64 v[18:19], 10, v[22:23]
	v_lshl_add_u64 v[18:19], s[42:43], 0, v[18:19]
	v_lshl_add_u64 v[18:19], v[18:19], 0, v[20:21]
	v_or_b32_e32 v26, 16, v22
	v_ashrrev_i32_e32 v27, 31, v26
	v_pk_fma_f32 v[30:31], v[190:191], s[48:49], v[14:15] op_sel_hi:[1,0,1]
	v_pk_fma_f32 v[34:35], v[186:187], s[48:49], v[10:11] op_sel_hi:[1,0,1]
	v_pk_fma_f32 v[32:33], v[188:189], s[48:49], v[12:13] op_sel_hi:[1,0,1]
	v_min_f32_e32 v34, 0x40e00000, v34
	v_min_f32_e32 v35, 0x40e00000, v35
	v_pk_mul_f32 v[56:57], v[34:35], s[50:51] op_sel_hi:[1,0]
	v_min_f32_e32 v30, 0x40e00000, v30
	v_exp_f32_e32 v56, v56
	v_exp_f32_e32 v57, v57
	v_min_f32_e32 v31, 0x40e00000, v31
	v_min_f32_e32 v32, 0x40e00000, v32
	v_min_f32_e32 v33, 0x40e00000, v33
	v_pk_mul_f32 v[52:53], v[30:31], s[50:51] op_sel_hi:[1,0]
	v_pk_mul_f32 v[58:59], v[32:33], s[50:51] op_sel_hi:[1,0]
	v_exp_f32_e32 v52, v52
	v_exp_f32_e32 v53, v53
	v_exp_f32_e32 v58, v58
	v_exp_f32_e32 v59, v59
	v_pk_add_f32 v[56:57], v[56:57], 1.0 op_sel_hi:[1,0]
	v_pk_fma_f32 v[28:29], v[192:193], s[48:49], v[16:17] op_sel_hi:[1,0,1]
	v_rcp_f32_e32 v56, v56
	v_rcp_f32_e32 v57, v57
	v_min_f32_e32 v28, 0x40e00000, v28
	v_min_f32_e32 v29, 0x40e00000, v29
	v_pk_fma_f32 v[50:51], v[154:155], s[48:49], v[6:7] op_sel_hi:[1,0,1]
	v_pk_mul_f32 v[54:55], v[28:29], s[50:51] op_sel_hi:[1,0]
	v_pk_add_f32 v[52:53], v[52:53], 1.0 op_sel_hi:[1,0]
	v_exp_f32_e32 v54, v54
	v_exp_f32_e32 v55, v55
	v_med3_f32 v50, v50, s83, v202
	v_med3_f32 v51, v51, s83, v202
	v_pk_add_f32 v[58:59], v[58:59], 1.0 op_sel_hi:[1,0]
	v_rcp_f32_e32 v52, v52
	v_rcp_f32_e32 v53, v53
	v_pk_add_f32 v[50:51], v[50:51], 1.0 op_sel_hi:[1,0]
	v_rcp_f32_e32 v58, v58
	v_rcp_f32_e32 v59, v59
	v_pk_mul_f32 v[34:35], v[34:35], v[56:57]
	v_pk_fma_f32 v[46:47], v[158:159], s[48:49], v[2:3] op_sel_hi:[1,0,1]
	v_pk_mul_f32 v[34:35], v[50:51], v[34:35]
	v_pk_fma_f32 v[48:49], v[156:157], s[48:49], v[8:9] op_sel_hi:[1,0,1]
	v_med3_f32 v46, v46, s83, v202
	v_med3_f32 v47, v47, s83, v202
	v_cvt_pk_fp8_f32 v25, v34, v35
	v_pk_fma_f32 v[38:39], v[182:183], s[48:49], v[14:15] op_sel_hi:[1,0,1]
	v_med3_f32 v48, v48, s83, v202
	v_med3_f32 v49, v49, s83, v202
	v_pk_add_f32 v[46:47], v[46:47], 1.0 op_sel_hi:[1,0]
	v_pk_add_f32 v[54:55], v[54:55], 1.0 op_sel_hi:[1,0]
	v_pk_mul_f32 v[30:31], v[30:31], v[52:53]
	v_min_f32_e32 v38, 0x40e00000, v38
	v_min_f32_e32 v39, 0x40e00000, v39
	v_pk_add_f32 v[48:49], v[48:49], 1.0 op_sel_hi:[1,0]
	v_rcp_f32_e32 v54, v54
	v_rcp_f32_e32 v55, v55
	v_pk_mul_f32 v[32:33], v[32:33], v[58:59]
	v_pk_mul_f32 v[30:31], v[46:47], v[30:31]
	v_pk_fma_f32 v[36:37], v[184:185], s[48:49], v[16:17] op_sel_hi:[1,0,1]
	v_pk_mul_f32 v[216:217], v[38:39], s[50:51] op_sel_hi:[1,0]
	v_cvt_pk_fp8_f32 v24, v30, v31
	v_pk_mul_f32 v[30:31], v[48:49], v[32:33]
	v_pk_fma_f32 v[44:45], v[160:161], s[48:49], v[4:5] op_sel_hi:[1,0,1]
	v_exp_f32_e32 v216, v216
	v_exp_f32_e32 v217, v217
	v_cvt_pk_fp8_f32 v25, v30, v31 op_sel:[0,0,1]
	v_min_f32_e32 v30, 0x40e00000, v36
	v_min_f32_e32 v31, 0x40e00000, v37
	v_med3_f32 v44, v44, s83, v202
	v_med3_f32 v45, v45, s83, v202
	v_pk_mul_f32 v[32:33], v[30:31], s[50:51] op_sel_hi:[1,0]
	v_pk_add_f32 v[44:45], v[44:45], 1.0 op_sel_hi:[1,0]
	v_pk_mul_f32 v[28:29], v[28:29], v[54:55]
	v_exp_f32_e32 v32, v32
	v_exp_f32_e32 v33, v33
	v_pk_mul_f32 v[28:29], v[44:45], v[28:29]
	v_pk_fma_f32 v[42:43], v[178:179], s[48:49], v[10:11] op_sel_hi:[1,0,1]
	v_cvt_pk_fp8_f32 v24, v28, v29 op_sel:[0,0,1]
	v_pk_add_f32 v[28:29], v[216:217], 1.0 op_sel_hi:[1,0]
	v_pk_add_f32 v[32:33], v[32:33], 1.0 op_sel_hi:[1,0]
	v_rcp_f32_e32 v28, v28
	v_rcp_f32_e32 v29, v29
	v_min_f32_e32 v34, 0x40e00000, v42
	v_min_f32_e32 v35, 0x40e00000, v43
	v_pk_fma_f32 v[62:63], v[150:151], s[48:49], v[2:3] op_sel_hi:[1,0,1]
	v_rcp_f32_e32 v32, v32
	v_rcp_f32_e32 v33, v33
	v_pk_mul_f32 v[36:37], v[34:35], s[50:51] op_sel_hi:[1,0]
	v_med3_f32 v62, v62, s83, v202
	v_med3_f32 v63, v63, s83, v202
	v_exp_f32_e32 v36, v36
	v_exp_f32_e32 v37, v37
	v_pk_fma_f32 v[60:61], v[152:153], s[48:49], v[4:5] op_sel_hi:[1,0,1]
	global_store_dwordx2 v[18:19], v[24:25], off
	v_pk_add_f32 v[24:25], v[62:63], 1.0 op_sel_hi:[1,0]
	v_pk_mul_f32 v[28:29], v[38:39], v[28:29]
	v_pk_mul_f32 v[30:31], v[30:31], v[32:33]
	v_pk_mul_f32 v[24:25], v[24:25], v[28:29]
	v_med3_f32 v28, v60, s83, v202
	v_med3_f32 v29, v61, s83, v202
	v_pk_add_f32 v[28:29], v[28:29], 1.0 op_sel_hi:[1,0]
	v_pk_fma_f32 v[40:41], v[180:181], s[48:49], v[12:13] op_sel_hi:[1,0,1]
	v_pk_mul_f32 v[28:29], v[28:29], v[30:31]
	v_pk_add_f32 v[30:31], v[36:37], 1.0 op_sel_hi:[1,0]
	v_mov_b32_e32 v38, 0
	v_rcp_f32_e32 v30, v30
	v_rcp_f32_e32 v31, v31
	v_cvt_pk_fp8_f32 v38, v24, v25
	v_pk_fma_f32 v[214:215], v[146:147], s[48:49], v[6:7] op_sel_hi:[1,0,1]
	v_mov_b32_e32 v39, 0
	v_pk_mul_f32 v[30:31], v[34:35], v[30:31]
	v_min_f32_e32 v34, 0x40e00000, v40
	v_min_f32_e32 v35, 0x40e00000, v41
	v_pk_mul_f32 v[36:37], v[34:35], s[50:51] op_sel_hi:[1,0]
	v_cvt_pk_fp8_f32 v38, v28, v29 op_sel:[0,0,1]
	v_exp_f32_e32 v36, v36
	v_exp_f32_e32 v37, v37
	v_pk_fma_f32 v[28:29], v[174:175], s[48:49], v[14:15] op_sel_hi:[1,0,1]
	v_med3_f32 v32, v214, s83, v202
	v_min_f32_e32 v28, 0x40e00000, v28
	v_pk_add_f32 v[36:37], v[36:37], 1.0 op_sel_hi:[1,0]
	v_min_f32_e32 v29, 0x40e00000, v29
	v_rcp_f32_e32 v36, v36
	v_rcp_f32_e32 v37, v37
	v_med3_f32 v33, v215, s83, v202
	v_pk_add_f32 v[32:33], v[32:33], 1.0 op_sel_hi:[1,0]
	v_pk_fma_f32 v[64:65], v[148:149], s[48:49], v[8:9] op_sel_hi:[1,0,1]
	v_pk_mul_f32 v[24:25], v[34:35], v[36:37]
	v_pk_mul_f32 v[36:37], v[28:29], s[50:51] op_sel_hi:[1,0]
	v_pk_mul_f32 v[30:31], v[32:33], v[30:31]
	v_exp_f32_e32 v36, v36
	v_exp_f32_e32 v37, v37
	v_cvt_pk_fp8_f32 v39, v30, v31
	v_med3_f32 v32, v64, s83, v202
	v_med3_f32 v33, v65, s83, v202
	v_pk_add_f32 v[36:37], v[36:37], 1.0 op_sel_hi:[1,0]
	v_pk_add_f32 v[32:33], v[32:33], 1.0 op_sel_hi:[1,0]
	v_rcp_f32_e32 v36, v36
	v_rcp_f32_e32 v37, v37
	v_pk_mul_f32 v[24:25], v[32:33], v[24:25]
	v_pk_fma_f32 v[32:33], v[170:171], s[48:49], v[10:11] op_sel_hi:[1,0,1]
	v_cvt_pk_fp8_f32 v39, v24, v25 op_sel:[0,0,1]
	v_lshlrev_b64 v[24:25], 10, v[26:27]
	v_pk_fma_f32 v[26:27], v[176:177], s[48:49], v[16:17] op_sel_hi:[1,0,1]
	v_pk_mul_f32 v[28:29], v[28:29], v[36:37]
	v_min_f32_e32 v26, 0x40e00000, v26
	v_min_f32_e32 v27, 0x40e00000, v27
	v_pk_mul_f32 v[36:37], v[26:27], s[50:51] op_sel_hi:[1,0]
	v_lshl_add_u64 v[24:25], s[42:43], 0, v[24:25]
	v_exp_f32_e32 v36, v36
	v_exp_f32_e32 v37, v37
	v_lshl_add_u64 v[24:25], v[24:25], 0, v[20:21]
	global_store_dwordx2 v[24:25], v[38:39], off
	v_pk_fma_f32 v[38:39], v[142:143], s[48:49], v[2:3] op_sel_hi:[1,0,1]
	v_pk_add_f32 v[36:37], v[36:37], 1.0 op_sel_hi:[1,0]
	v_med3_f32 v38, v38, s83, v202
	v_med3_f32 v39, v39, s83, v202
	v_pk_add_f32 v[38:39], v[38:39], 1.0 op_sel_hi:[1,0]
	v_min_f32_e32 v32, 0x40e00000, v32
	v_min_f32_e32 v33, 0x40e00000, v33
	v_pk_mul_f32 v[28:29], v[38:39], v[28:29]
	v_rcp_f32_e32 v36, v36
	v_rcp_f32_e32 v37, v37
	v_pk_mul_f32 v[38:39], v[32:33], s[50:51] op_sel_hi:[1,0]
	v_pk_fma_f32 v[34:35], v[144:145], s[48:49], v[4:5] op_sel_hi:[1,0,1]
	v_exp_f32_e32 v38, v38
	v_exp_f32_e32 v39, v39
	v_med3_f32 v34, v34, s83, v202
	v_med3_f32 v35, v35, s83, v202
	v_pk_add_f32 v[34:35], v[34:35], 1.0 op_sel_hi:[1,0]
	v_pk_mul_f32 v[26:27], v[26:27], v[36:37]
	v_pk_fma_f32 v[30:31], v[172:173], s[48:49], v[12:13] op_sel_hi:[1,0,1]
	v_pk_mul_f32 v[26:27], v[34:35], v[26:27]
	v_pk_add_f32 v[34:35], v[38:39], 1.0 op_sel_hi:[1,0]
	v_min_f32_e32 v30, 0x40e00000, v30
	v_rcp_f32_e32 v34, v34
	v_rcp_f32_e32 v35, v35
	v_min_f32_e32 v31, 0x40e00000, v31
	v_mov_b32_e32 v38, 0
	v_cvt_pk_fp8_f32 v38, v28, v29
	v_pk_mul_f32 v[32:33], v[32:33], v[34:35]
	v_pk_mul_f32 v[34:35], v[30:31], s[50:51] op_sel_hi:[1,0]
	v_pk_fma_f32 v[42:43], v[138:139], s[48:49], v[6:7] op_sel_hi:[1,0,1]
	v_exp_f32_e32 v34, v34
	v_exp_f32_e32 v35, v35
	v_med3_f32 v36, v42, s83, v202
	v_med3_f32 v37, v43, s83, v202
	v_pk_add_f32 v[36:37], v[36:37], 1.0 op_sel_hi:[1,0]
	v_pk_add_f32 v[34:35], v[34:35], 1.0 op_sel_hi:[1,0]
	v_cvt_pk_fp8_f32 v38, v26, v27 op_sel:[0,0,1]
	v_rcp_f32_e32 v34, v34
	v_rcp_f32_e32 v35, v35
	v_pk_fma_f32 v[26:27], v[166:167], s[48:49], v[14:15] op_sel_hi:[1,0,1]
	v_pk_mul_f32 v[32:33], v[36:37], v[32:33]
	v_mov_b32_e32 v39, 0
	v_min_f32_e32 v26, 0x40e00000, v26
	v_min_f32_e32 v27, 0x40e00000, v27
	v_pk_fma_f32 v[40:41], v[140:141], s[48:49], v[8:9] op_sel_hi:[1,0,1]
	v_cvt_pk_fp8_f32 v39, v32, v33
	v_pk_mul_f32 v[28:29], v[30:31], v[34:35]
	v_pk_mul_f32 v[34:35], v[26:27], s[50:51] op_sel_hi:[1,0]
	v_med3_f32 v36, v40, s83, v202
	v_med3_f32 v37, v41, s83, v202
	v_exp_f32_e32 v34, v34
	v_exp_f32_e32 v35, v35
	v_pk_add_f32 v[36:37], v[36:37], 1.0 op_sel_hi:[1,0]
	v_or_b32_e32 v24, 32, v22
	v_pk_mul_f32 v[28:29], v[36:37], v[28:29]
	v_ashrrev_i32_e32 v25, 31, v24
	v_cvt_pk_fp8_f32 v39, v28, v29 op_sel:[0,0,1]
	v_lshlrev_b64 v[24:25], 10, v[24:25]
	v_pk_add_f32 v[34:35], v[34:35], 1.0 op_sel_hi:[1,0]
	v_lshl_add_u64 v[24:25], s[42:43], 0, v[24:25]
	v_rcp_f32_e32 v34, v34
	v_rcp_f32_e32 v35, v35
	v_lshl_add_u64 v[24:25], v[24:25], 0, v[20:21]
	global_store_dwordx2 v[24:25], v[38:39], off
	v_pk_fma_f32 v[24:25], v[168:169], s[48:49], v[16:17] op_sel_hi:[1,0,1]
	v_pk_mul_f32 v[26:27], v[26:27], v[34:35]
	v_min_f32_e32 v24, 0x40e00000, v24
	v_min_f32_e32 v25, 0x40e00000, v25
	v_pk_mul_f32 v[34:35], v[24:25], s[50:51] op_sel_hi:[1,0]
	v_pk_fma_f32 v[36:37], v[134:135], s[48:49], v[2:3] op_sel_hi:[1,0,1]
	v_exp_f32_e32 v34, v34
	v_exp_f32_e32 v35, v35
	v_pk_fma_f32 v[30:31], v[162:163], s[48:49], v[10:11] op_sel_hi:[1,0,1]
	v_med3_f32 v36, v36, s83, v202
	v_med3_f32 v37, v37, s83, v202
	v_pk_add_f32 v[36:37], v[36:37], 1.0 op_sel_hi:[1,0]
	v_pk_add_f32 v[34:35], v[34:35], 1.0 op_sel_hi:[1,0]
	v_min_f32_e32 v30, 0x40e00000, v30
	v_min_f32_e32 v31, 0x40e00000, v31
	v_pk_mul_f32 v[26:27], v[36:37], v[26:27]
	v_rcp_f32_e32 v34, v34
	v_rcp_f32_e32 v35, v35
	v_pk_mul_f32 v[36:37], v[30:31], s[50:51] op_sel_hi:[1,0]
	v_pk_fma_f32 v[32:33], v[136:137], s[48:49], v[4:5] op_sel_hi:[1,0,1]
	v_exp_f32_e32 v36, v36
	v_exp_f32_e32 v37, v37
	v_med3_f32 v32, v32, s83, v202
	v_med3_f32 v33, v33, s83, v202
	v_pk_add_f32 v[32:33], v[32:33], 1.0 op_sel_hi:[1,0]
	v_pk_mul_f32 v[24:25], v[24:25], v[34:35]
	v_pk_fma_f32 v[28:29], v[164:165], s[48:49], v[12:13] op_sel_hi:[1,0,1]
	v_pk_mul_f32 v[24:25], v[32:33], v[24:25]
	v_pk_add_f32 v[32:33], v[36:37], 1.0 op_sel_hi:[1,0]
	v_min_f32_e32 v28, 0x40e00000, v28
	v_rcp_f32_e32 v32, v32
	v_rcp_f32_e32 v33, v33
	v_min_f32_e32 v29, 0x40e00000, v29
	v_or_b32_e32 v22, 48, v22
	v_ashrrev_i32_e32 v23, 31, v22
	v_pk_mul_f32 v[30:31], v[30:31], v[32:33]
	v_pk_mul_f32 v[32:33], v[28:29], s[50:51] op_sel_hi:[1,0]
	v_pk_fma_f32 v[40:41], v[130:131], s[48:49], v[6:7] op_sel_hi:[1,0,1]
	v_exp_f32_e32 v32, v32
	v_exp_f32_e32 v33, v33
	v_lshlrev_b64 v[22:23], 10, v[22:23]
	v_med3_f32 v34, v40, s83, v202
	v_med3_f32 v35, v41, s83, v202
	v_pk_add_f32 v[32:33], v[32:33], 1.0 op_sel_hi:[1,0]
	v_lshl_add_u64 v[22:23], s[42:43], 0, v[22:23]
	v_pk_add_f32 v[34:35], v[34:35], 1.0 op_sel_hi:[1,0]
	v_rcp_f32_e32 v32, v32
	v_rcp_f32_e32 v33, v33
	v_lshl_add_u64 v[20:21], v[22:23], 0, v[20:21]
	v_pk_fma_f32 v[22:23], v[126:127], s[48:49], v[14:15] op_sel_hi:[1,0,1]
	v_pk_mul_f32 v[30:31], v[34:35], v[30:31]
	v_mov_b32_e32 v36, 0
	v_mov_b32_e32 v37, 0
	v_min_f32_e32 v22, 0x40e00000, v22
	v_min_f32_e32 v23, 0x40e00000, v23
	v_pk_fma_f32 v[38:39], v[132:133], s[48:49], v[8:9] op_sel_hi:[1,0,1]
	v_cvt_pk_fp8_f32 v36, v26, v27
	v_cvt_pk_fp8_f32 v37, v30, v31
	v_pk_mul_f32 v[30:31], v[22:23], s[50:51] op_sel_hi:[1,0]
	v_med3_f32 v34, v38, s83, v202
	v_med3_f32 v35, v39, s83, v202
	v_exp_f32_e32 v30, v30
	v_exp_f32_e32 v31, v31
	v_pk_add_f32 v[34:35], v[34:35], 1.0 op_sel_hi:[1,0]
	v_pk_mul_f32 v[26:27], v[28:29], v[32:33]
	v_cvt_pk_fp8_f32 v36, v24, v25 op_sel:[0,0,1]
	v_pk_mul_f32 v[26:27], v[34:35], v[26:27]
	v_pk_add_f32 v[30:31], v[30:31], 1.0 op_sel_hi:[1,0]
	v_cvt_pk_fp8_f32 v37, v26, v27 op_sel:[0,0,1]
	v_rcp_f32_e32 v30, v30
	v_rcp_f32_e32 v31, v31
	v_pk_fma_f32 v[32:33], v[94:95], s[48:49], v[2:3] op_sel_hi:[1,0,1]
	global_store_dwordx2 v[20:21], v[36:37], off
	v_pk_fma_f32 v[20:21], v[128:129], s[48:49], v[16:17] op_sel_hi:[1,0,1]
	v_pk_mul_f32 v[22:23], v[22:23], v[30:31]
	v_min_f32_e32 v20, 0x40e00000, v20
	v_min_f32_e32 v21, 0x40e00000, v21
	v_pk_mul_f32 v[30:31], v[20:21], s[50:51] op_sel_hi:[1,0]
	v_pk_fma_f32 v[26:27], v[122:123], s[48:49], v[10:11] op_sel_hi:[1,0,1]
	v_exp_f32_e32 v30, v30
	v_exp_f32_e32 v31, v31
	v_med3_f32 v32, v32, s83, v202
	v_med3_f32 v33, v33, s83, v202
	v_pk_add_f32 v[32:33], v[32:33], 1.0 op_sel_hi:[1,0]
	v_pk_add_f32 v[30:31], v[30:31], 1.0 op_sel_hi:[1,0]
	v_min_f32_e32 v26, 0x40e00000, v26
	v_min_f32_e32 v27, 0x40e00000, v27
	v_pk_mul_f32 v[22:23], v[32:33], v[22:23]
	v_rcp_f32_e32 v30, v30
	v_rcp_f32_e32 v31, v31
	v_pk_mul_f32 v[32:33], v[26:27], s[50:51] op_sel_hi:[1,0]
	v_pk_fma_f32 v[28:29], v[96:97], s[48:49], v[4:5] op_sel_hi:[1,0,1]
	v_exp_f32_e32 v32, v32
	v_exp_f32_e32 v33, v33
	v_med3_f32 v28, v28, s83, v202
	v_med3_f32 v29, v29, s83, v202
	v_pk_add_f32 v[28:29], v[28:29], 1.0 op_sel_hi:[1,0]
	v_pk_mul_f32 v[20:21], v[20:21], v[30:31]
	v_pk_fma_f32 v[24:25], v[124:125], s[48:49], v[12:13] op_sel_hi:[1,0,1]
	v_pk_mul_f32 v[20:21], v[28:29], v[20:21]
	v_pk_add_f32 v[28:29], v[32:33], 1.0 op_sel_hi:[1,0]
	v_min_f32_e32 v24, 0x40e00000, v24
	v_rcp_f32_e32 v28, v28
	v_rcp_f32_e32 v29, v29
	v_min_f32_e32 v25, 0x40e00000, v25
	v_pk_fma_f32 v[36:37], v[90:91], s[48:49], v[6:7] op_sel_hi:[1,0,1]
	v_mov_b32_e32 v33, 0
	v_pk_mul_f32 v[26:27], v[26:27], v[28:29]
	v_pk_mul_f32 v[28:29], v[24:25], s[50:51] op_sel_hi:[1,0]
	v_med3_f32 v30, v36, s83, v202
	v_exp_f32_e32 v28, v28
	v_exp_f32_e32 v29, v29
	v_med3_f32 v31, v37, s83, v202
	v_pk_add_f32 v[30:31], v[30:31], 1.0 op_sel_hi:[1,0]
	v_pk_fma_f32 v[34:35], v[92:93], s[48:49], v[8:9] op_sel_hi:[1,0,1]
	v_pk_add_f32 v[28:29], v[28:29], 1.0 op_sel_hi:[1,0]
	v_pk_mul_f32 v[26:27], v[30:31], v[26:27]
	v_rcp_f32_e32 v28, v28
	v_rcp_f32_e32 v29, v29
	v_cvt_pk_fp8_f32 v33, v26, v27
	v_med3_f32 v30, v34, s83, v202
	v_med3_f32 v31, v35, s83, v202
	v_mov_b32_e32 v32, 0
	v_pk_add_f32 v[30:31], v[30:31], 1.0 op_sel_hi:[1,0]
	v_cvt_pk_fp8_f32 v32, v22, v23
	v_pk_mul_f32 v[22:23], v[24:25], v[28:29]
	v_pk_fma_f32 v[26:27], v[114:115], s[48:49], v[10:11] op_sel_hi:[1,0,1]
	v_pk_mul_f32 v[22:23], v[30:31], v[22:23]
	v_cvt_pk_fp8_f32 v32, v20, v21 op_sel:[0,0,1]
	v_cvt_pk_fp8_f32 v33, v22, v23 op_sel:[0,0,1]
	v_pk_fma_f32 v[22:23], v[118:119], s[48:49], v[14:15] op_sel_hi:[1,0,1]
	v_add_co_u32_e32 v20, vcc, s81, v18
	v_min_f32_e32 v22, 0x40e00000, v22
	v_min_f32_e32 v23, 0x40e00000, v23
	v_pk_mul_f32 v[30:31], v[22:23], s[50:51] op_sel_hi:[1,0]
	v_addc_co_u32_e32 v21, vcc, 0, v19, vcc
	v_exp_f32_e32 v30, v30
	v_exp_f32_e32 v31, v31
	global_store_dwordx2 v[20:21], v[32:33], off
	v_pk_fma_f32 v[20:21], v[120:121], s[48:49], v[16:17] op_sel_hi:[1,0,1]
	v_pk_fma_f32 v[32:33], v[86:87], s[48:49], v[2:3] op_sel_hi:[1,0,1]
	v_pk_add_f32 v[30:31], v[30:31], 1.0 op_sel_hi:[1,0]
	v_min_f32_e32 v20, 0x40e00000, v20
	v_rcp_f32_e32 v30, v30
	v_rcp_f32_e32 v31, v31
	v_min_f32_e32 v21, 0x40e00000, v21
	v_med3_f32 v32, v32, s83, v202
	v_med3_f32 v33, v33, s83, v202
	v_pk_mul_f32 v[22:23], v[22:23], v[30:31]
	v_pk_mul_f32 v[30:31], v[20:21], s[50:51] op_sel_hi:[1,0]
	v_pk_add_f32 v[32:33], v[32:33], 1.0 op_sel_hi:[1,0]
	v_exp_f32_e32 v30, v30
	v_exp_f32_e32 v31, v31
	v_min_f32_e32 v26, 0x40e00000, v26
	v_min_f32_e32 v27, 0x40e00000, v27
	v_pk_mul_f32 v[22:23], v[32:33], v[22:23]
	v_pk_add_f32 v[30:31], v[30:31], 1.0 op_sel_hi:[1,0]
	v_pk_mul_f32 v[32:33], v[26:27], s[50:51] op_sel_hi:[1,0]
	v_rcp_f32_e32 v30, v30
	v_rcp_f32_e32 v31, v31
	v_exp_f32_e32 v32, v32
	v_exp_f32_e32 v33, v33
	v_pk_fma_f32 v[28:29], v[88:89], s[48:49], v[4:5] op_sel_hi:[1,0,1]
	v_pk_mul_f32 v[20:21], v[20:21], v[30:31]
	v_med3_f32 v28, v28, s83, v202
	v_med3_f32 v29, v29, s83, v202
	v_pk_add_f32 v[28:29], v[28:29], 1.0 op_sel_hi:[1,0]
	v_pk_fma_f32 v[24:25], v[116:117], s[48:49], v[12:13] op_sel_hi:[1,0,1]
	v_pk_mul_f32 v[20:21], v[28:29], v[20:21]
	v_pk_add_f32 v[28:29], v[32:33], 1.0 op_sel_hi:[1,0]
	v_min_f32_e32 v24, 0x40e00000, v24
	v_rcp_f32_e32 v28, v28
	v_rcp_f32_e32 v29, v29
	v_min_f32_e32 v25, 0x40e00000, v25
	v_pk_fma_f32 v[36:37], v[82:83], s[48:49], v[6:7] op_sel_hi:[1,0,1]
	v_mov_b32_e32 v33, 0
	v_pk_mul_f32 v[26:27], v[26:27], v[28:29]
	v_pk_mul_f32 v[28:29], v[24:25], s[50:51] op_sel_hi:[1,0]
	v_med3_f32 v30, v36, s83, v202
	v_exp_f32_e32 v28, v28
	v_exp_f32_e32 v29, v29
	v_med3_f32 v31, v37, s83, v202
	v_pk_add_f32 v[30:31], v[30:31], 1.0 op_sel_hi:[1,0]
	v_pk_fma_f32 v[34:35], v[84:85], s[48:49], v[8:9] op_sel_hi:[1,0,1]
	v_pk_add_f32 v[28:29], v[28:29], 1.0 op_sel_hi:[1,0]
	v_pk_mul_f32 v[26:27], v[30:31], v[26:27]
	v_rcp_f32_e32 v28, v28
	v_rcp_f32_e32 v29, v29
	v_cvt_pk_fp8_f32 v33, v26, v27
	v_med3_f32 v30, v34, s83, v202
	v_med3_f32 v31, v35, s83, v202
	v_mov_b32_e32 v32, 0
	v_pk_add_f32 v[30:31], v[30:31], 1.0 op_sel_hi:[1,0]
	v_cvt_pk_fp8_f32 v32, v22, v23
	v_pk_mul_f32 v[22:23], v[24:25], v[28:29]
	v_pk_fma_f32 v[26:27], v[106:107], s[48:49], v[10:11] op_sel_hi:[1,0,1]
	v_pk_mul_f32 v[22:23], v[30:31], v[22:23]
	v_cvt_pk_fp8_f32 v32, v20, v21 op_sel:[0,0,1]
	v_cvt_pk_fp8_f32 v33, v22, v23 op_sel:[0,0,1]
	v_pk_fma_f32 v[22:23], v[110:111], s[48:49], v[14:15] op_sel_hi:[1,0,1]
	v_add_co_u32_e32 v20, vcc, s84, v18
	v_min_f32_e32 v22, 0x40e00000, v22
	v_min_f32_e32 v23, 0x40e00000, v23
	v_pk_mul_f32 v[30:31], v[22:23], s[50:51] op_sel_hi:[1,0]
	v_addc_co_u32_e32 v21, vcc, 0, v19, vcc
	v_exp_f32_e32 v30, v30
	v_exp_f32_e32 v31, v31
	global_store_dwordx2 v[20:21], v[32:33], off
	v_pk_fma_f32 v[20:21], v[112:113], s[48:49], v[16:17] op_sel_hi:[1,0,1]
	v_pk_fma_f32 v[32:33], v[78:79], s[48:49], v[2:3] op_sel_hi:[1,0,1]
	v_pk_add_f32 v[30:31], v[30:31], 1.0 op_sel_hi:[1,0]
	v_min_f32_e32 v20, 0x40e00000, v20
	v_rcp_f32_e32 v30, v30
	v_rcp_f32_e32 v31, v31
	v_min_f32_e32 v21, 0x40e00000, v21
	v_med3_f32 v32, v32, s83, v202
	v_med3_f32 v33, v33, s83, v202
	v_pk_mul_f32 v[22:23], v[22:23], v[30:31]
	v_pk_mul_f32 v[30:31], v[20:21], s[50:51] op_sel_hi:[1,0]
	v_pk_add_f32 v[32:33], v[32:33], 1.0 op_sel_hi:[1,0]
	v_exp_f32_e32 v30, v30
	v_exp_f32_e32 v31, v31
	v_min_f32_e32 v26, 0x40e00000, v26
	v_min_f32_e32 v27, 0x40e00000, v27
	v_pk_mul_f32 v[22:23], v[32:33], v[22:23]
	v_pk_add_f32 v[30:31], v[30:31], 1.0 op_sel_hi:[1,0]
	v_pk_mul_f32 v[32:33], v[26:27], s[50:51] op_sel_hi:[1,0]
	v_rcp_f32_e32 v30, v30
	v_rcp_f32_e32 v31, v31
	v_exp_f32_e32 v32, v32
	v_exp_f32_e32 v33, v33
	v_pk_fma_f32 v[28:29], v[80:81], s[48:49], v[4:5] op_sel_hi:[1,0,1]
	v_pk_mul_f32 v[20:21], v[20:21], v[30:31]
	v_med3_f32 v28, v28, s83, v202
	v_med3_f32 v29, v29, s83, v202
	v_pk_add_f32 v[28:29], v[28:29], 1.0 op_sel_hi:[1,0]
	v_pk_fma_f32 v[24:25], v[108:109], s[48:49], v[12:13] op_sel_hi:[1,0,1]
	v_pk_mul_f32 v[20:21], v[28:29], v[20:21]
	v_pk_add_f32 v[28:29], v[32:33], 1.0 op_sel_hi:[1,0]
	v_min_f32_e32 v24, 0x40e00000, v24
	v_rcp_f32_e32 v28, v28
	v_rcp_f32_e32 v29, v29
	v_min_f32_e32 v25, 0x40e00000, v25
	v_pk_fma_f32 v[36:37], v[74:75], s[48:49], v[6:7] op_sel_hi:[1,0,1]
	v_mov_b32_e32 v32, 0
	v_pk_mul_f32 v[26:27], v[26:27], v[28:29]
	v_pk_mul_f32 v[28:29], v[24:25], s[50:51] op_sel_hi:[1,0]
	v_med3_f32 v30, v36, s83, v202
	v_exp_f32_e32 v28, v28
	v_exp_f32_e32 v29, v29
	v_med3_f32 v31, v37, s83, v202
	v_pk_add_f32 v[30:31], v[30:31], 1.0 op_sel_hi:[1,0]
	v_mov_b32_e32 v33, 0
	v_pk_add_f32 v[28:29], v[28:29], 1.0 op_sel_hi:[1,0]
	v_pk_mul_f32 v[26:27], v[30:31], v[26:27]
	v_rcp_f32_e32 v28, v28
	v_rcp_f32_e32 v29, v29
	v_pk_fma_f32 v[34:35], v[76:77], s[48:49], v[8:9] op_sel_hi:[1,0,1]
	v_cvt_pk_fp8_f32 v32, v22, v23
	v_cvt_pk_fp8_f32 v33, v26, v27
	v_med3_f32 v30, v34, s83, v202
	v_med3_f32 v31, v35, s83, v202
	v_pk_add_f32 v[30:31], v[30:31], 1.0 op_sel_hi:[1,0]
	v_pk_mul_f32 v[22:23], v[24:25], v[28:29]
	v_cvt_pk_fp8_f32 v32, v20, v21 op_sel:[0,0,1]
	v_pk_mul_f32 v[22:23], v[30:31], v[22:23]
	v_add_co_u32_e32 v20, vcc, s85, v18
	v_cvt_pk_fp8_f32 v33, v22, v23 op_sel:[0,0,1]
	v_pk_fma_f32 v[14:15], v[102:103], s[48:49], v[14:15] op_sel_hi:[1,0,1]
	v_addc_co_u32_e32 v21, vcc, 0, v19, vcc
	v_min_f32_e32 v14, 0x40e00000, v14
	v_min_f32_e32 v15, 0x40e00000, v15
	global_store_dwordx2 v[20:21], v[32:33], off
	v_pk_mul_f32 v[20:21], v[14:15], s[50:51] op_sel_hi:[1,0]
	v_pk_fma_f32 v[16:17], v[104:105], s[48:49], v[16:17] op_sel_hi:[1,0,1]
	v_exp_f32_e32 v20, v20
	v_exp_f32_e32 v21, v21
	v_min_f32_e32 v16, 0x40e00000, v16
	v_min_f32_e32 v17, 0x40e00000, v17
	v_pk_fma_f32 v[2:3], v[70:71], s[48:49], v[2:3] op_sel_hi:[1,0,1]
	v_pk_add_f32 v[20:21], v[20:21], 1.0 op_sel_hi:[1,0]
	v_med3_f32 v2, v2, s83, v202
	v_rcp_f32_e32 v20, v20
	v_rcp_f32_e32 v21, v21
	v_med3_f32 v3, v3, s83, v202
	v_pk_fma_f32 v[10:11], v[98:99], s[48:49], v[10:11] op_sel_hi:[1,0,1]
	v_pk_add_f32 v[2:3], v[2:3], 1.0 op_sel_hi:[1,0]
	v_pk_mul_f32 v[14:15], v[14:15], v[20:21]
	v_pk_mul_f32 v[20:21], v[16:17], s[50:51] op_sel_hi:[1,0]
	v_pk_mul_f32 v[2:3], v[2:3], v[14:15]
	v_exp_f32_e32 v20, v20
	v_exp_f32_e32 v21, v21
	v_min_f32_e32 v10, 0x40e00000, v10
	v_min_f32_e32 v11, 0x40e00000, v11
	v_pk_fma_f32 v[4:5], v[72:73], s[48:49], v[4:5] op_sel_hi:[1,0,1]
	v_pk_add_f32 v[14:15], v[20:21], 1.0 op_sel_hi:[1,0]
	v_pk_mul_f32 v[20:21], v[10:11], s[50:51] op_sel_hi:[1,0]
	v_rcp_f32_e32 v14, v14
	v_rcp_f32_e32 v15, v15
	v_exp_f32_e32 v20, v20
	v_exp_f32_e32 v21, v21
	v_med3_f32 v4, v4, s83, v202
	v_med3_f32 v5, v5, s83, v202
	v_pk_add_f32 v[4:5], v[4:5], 1.0 op_sel_hi:[1,0]
	v_pk_mul_f32 v[14:15], v[16:17], v[14:15]
	v_pk_fma_f32 v[12:13], v[100:101], s[48:49], v[12:13] op_sel_hi:[1,0,1]
	v_pk_mul_f32 v[4:5], v[4:5], v[14:15]
	v_pk_add_f32 v[14:15], v[20:21], 1.0 op_sel_hi:[1,0]
	v_min_f32_e32 v12, 0x40e00000, v12
	v_rcp_f32_e32 v14, v14
	v_rcp_f32_e32 v15, v15
	v_min_f32_e32 v13, 0x40e00000, v13
	v_pk_fma_f32 v[6:7], v[66:67], s[48:49], v[6:7] op_sel_hi:[1,0,1]
	v_pk_fma_f32 v[8:9], v[68:69], s[48:49], v[8:9] op_sel_hi:[1,0,1]
	v_pk_mul_f32 v[10:11], v[10:11], v[14:15]
	v_pk_mul_f32 v[14:15], v[12:13], s[50:51] op_sel_hi:[1,0]
	v_med3_f32 v6, v6, s83, v202
	v_exp_f32_e32 v14, v14
	v_exp_f32_e32 v15, v15
	v_med3_f32 v7, v7, s83, v202
	v_pk_add_f32 v[6:7], v[6:7], 1.0 op_sel_hi:[1,0]
	v_med3_f32 v8, v8, s83, v202
	v_pk_mul_f32 v[6:7], v[6:7], v[10:11]
	v_pk_add_f32 v[10:11], v[14:15], 1.0 op_sel_hi:[1,0]
	v_mov_b32_e32 v14, 0
	v_rcp_f32_e32 v10, v10
	v_rcp_f32_e32 v11, v11
	v_mov_b32_e32 v15, 0
	v_cvt_pk_fp8_f32 v14, v2, v3
	v_cvt_pk_fp8_f32 v15, v6, v7
	v_med3_f32 v9, v9, s83, v202
	v_pk_add_f32 v[8:9], v[8:9], 1.0 op_sel_hi:[1,0]
	v_pk_mul_f32 v[2:3], v[12:13], v[10:11]
	v_cvt_pk_fp8_f32 v14, v4, v5 op_sel:[0,0,1]
	v_pk_mul_f32 v[2:3], v[8:9], v[2:3]
	v_mov_b32_e32 v5, v213
	v_cvt_pk_fp8_f32 v15, v2, v3 op_sel:[0,0,1]
	v_add_co_u32_e32 v2, vcc, 0x2c000, v18
	v_mov_b32_e32 v4, v211
	s_nop 0
	v_addc_co_u32_e32 v3, vcc, 0, v19, vcc
	global_store_dwordx2 v[2:3], v[14:15], off
	s_and_b64 vcc, exec, s[4:5]
	v_mov_b32_e32 v2, v212
	v_mov_b32_e32 v3, v210
	s_cbranch_vccnz .LBB0_1794
	s_waitcnt vmcnt(8)
	v_mov_b32_e32 v2, v1
	s_nop 0
	v_ashrrev_i32_e32 v3, 31, v2
	v_lshrrev_b32_e32 v3, 26, v3
	v_lshlrev_b32_e32 v4, 4, v2
	v_add_u32_e32 v3, v2, v3
	v_bfe_i32 v2, v2, 27, 1
	v_lshrrev_b32_e32 v2, 22, v2
	v_add_u32_e32 v2, v4, v2
	v_and_b32_e32 v2, 0xfffffc00, v2
	v_sub_u32_e32 v2, v4, v2
	v_lshrrev_b32_e32 v5, 4, v2
	v_bitop3_b32 v5, v5, v2, 32 bitop3:0x6c
	v_ashrrev_i32_e32 v2, 31, v2
	v_lshrrev_b32_e32 v2, 26, v2
	v_add_u32_e32 v2, v5, v2
	v_and_b32_e32 v2, 0xc0, v2
	v_add_u32_e32 v4, 0x2000, v4
	v_sub_u32_e32 v2, v5, v2
	v_ashrrev_i32_e32 v5, 31, v4
	v_lshrrev_b32_e32 v5, 22, v5
	v_add_u32_e32 v5, v4, v5
	v_ashrrev_i32_e32 v5, 10, v5
	v_mul_i32_i24_e32 v6, 0x400, v5
	v_sub_u32_e32 v4, v4, v6
	v_lshrrev_b32_e32 v6, 4, v4
	v_bitop3_b32 v6, v6, v4, 32 bitop3:0x6c
	v_ashrrev_i32_e32 v4, 31, v4
	v_lshrrev_b32_e32 v4, 26, v4
	v_add_u32_e32 v4, v6, v4
	v_and_b32_e32 v4, 0xc0, v4
	v_sub_u32_e32 v4, v6, v4
	v_lshrrev_b32_e32 v3, 1, v3
	v_ashrrev_i16_sdwa v2, v194, sext(v2) dst_sel:DWORD dst_unused:UNUSED_PAD src0_sel:DWORD src1_sel:BYTE_0
	v_lshlrev_b32_e32 v5, 5, v5
	v_ashrrev_i16_sdwa v4, v194, sext(v4) dst_sel:DWORD dst_unused:UNUSED_PAD src0_sel:DWORD src1_sel:BYTE_0
	v_and_b32_e32 v3, 32, v3
	v_bfe_i32 v2, v2, 0, 16
	v_and_b32_e32 v5, 32, v5
	v_bfe_i32 v4, v4, 0, 16
	v_add_lshl_u32 v2, v3, v2, 1
	v_add_lshl_u32 v5, v5, v4, 1
	v_lshl_add_u32 v3, v204, 10, v2
	v_lshl_add_u32 v2, v203, 10, v2
	v_lshl_add_u32 v4, v207, 10, v5
	v_lshl_add_u32 v5, v206, 10, v5
